# MoBA step loops: packed f32 adds (bias add, exp sums) split into single v_add_f32 (packed VOP3P beside partner-wave MFMAs)
# baseline (speedup 1.0000x reference)
; __device__ __forceinline__ float fast_exp2(float x) { return __builtin_amdgcn_exp2f(x); }
; #define PK8(P, B) __builtin_bit_cast(bf16x8, (u32x4){pk_bf16(P[B], P[B + 1]), pk_bf16(P[B + 2], P[B + 3]), pk_bf16(P[B + 4], P[B + 5]), pk_bf16(P[B + 6], P[B + 7])})
; __device__ __forceinline__ void softmax_pv2(f32x16& a0, f32x16& a1, f32x16& b0, f32x16& b1, f32x16 (&o)[2], float& mref, float& l, f32x16& cn, bool first, LAS float* wsf, ...
;     ...
;     float s0 = 0.f, s1 = 0.f, s2 = 0.f, s3 = 0.f;
; #pragma unroll
;     for (int r = 0; r < 16; ++r) { a0[r] = fast_exp2(a0[r]); a1[r] = fast_exp2(a1[r]); b0[r] = fast_exp2(b0[r]); b1[r] = fast_exp2(b1[r]); s0 += a0[r]; s1 += a1[r]; s2 += b0[r]; s3 += b1[r]; }
;     l += (s0 + s1) + (s2 + s3);
;     bf16x8 pa[8];
;     ...
;     pa[0] = PK8(a0, 0); pa[1] = PK8(a0, 8); pa[2] = PK8(a1, 0); pa[3] = PK8(a1, 8); pa[4] = PK8(b0, 0); pa[5] = PK8(b0, 8); pa[6] = PK8(b1, 0); pa[7] = PK8(b1, 8);
.LBB0_646:
	v_exp_f32_e32 v141, v80
	v_exp_f32_e32 v143, v64
	v_exp_f32_e32 v142, v96
	v_exp_f32_e32 v140, v48
	v_exp_f32_e32 v81, v81
	v_exp_f32_e32 v65, v65
	v_exp_f32_e32 v64, v97
	v_exp_f32_e32 v80, v49
	v_exp_f32_e32 v97, v82
	v_exp_f32_e32 v145, v66
	v_exp_f32_e32 v144, v98
	v_exp_f32_e32 v96, v50
	v_exp_f32_e32 v83, v83
	v_exp_f32_e32 v67, v67
	v_exp_f32_e32 v66, v99
	v_exp_f32_e32 v82, v51
	v_exp_f32_e32 v99, v84
	v_exp_f32_e32 v147, v68
	v_exp_f32_e32 v146, v100
	v_exp_f32_e32 v98, v52
	v_add_f32_e32 v48, 0, v142
	v_add_f32_e32 v49, 0, v143
	v_add_f32_e32 v50, 0, v140
	v_add_f32_e32 v51, 0, v141
	v_add_f32_e32 v48, v64, v48
	v_add_f32_e32 v49, v65, v49
	v_add_f32_e32 v50, v80, v50
	v_add_f32_e32 v51, v81, v51
	v_exp_f32_e32 v85, v85
	v_exp_f32_e32 v69, v69
	v_exp_f32_e32 v68, v101
	v_exp_f32_e32 v84, v53
	v_add_f32_e32 v48, v144, v48
	v_add_f32_e32 v49, v145, v49
	v_add_f32_e32 v50, v96, v50
	v_add_f32_e32 v51, v97, v51
	v_exp_f32_e32 v101, v86
	v_exp_f32_e32 v149, v70
	v_exp_f32_e32 v148, v102
	v_exp_f32_e32 v100, v54
	v_add_f32_e32 v48, v66, v48
	v_add_f32_e32 v49, v67, v49
	v_add_f32_e32 v50, v82, v50
	v_add_f32_e32 v51, v83, v51
	v_exp_f32_e32 v87, v87
	v_exp_f32_e32 v71, v71
	v_exp_f32_e32 v70, v103
	v_exp_f32_e32 v86, v55
	v_add_f32_e32 v48, v146, v48
	v_add_f32_e32 v49, v147, v49
	v_add_f32_e32 v50, v98, v50
	v_add_f32_e32 v51, v99, v51
	v_exp_f32_e32 v151, v88
	v_exp_f32_e32 v103, v72
	v_exp_f32_e32 v102, v104
	v_exp_f32_e32 v150, v56
	v_exp_f32_e32 v153, v89
	v_exp_f32_e32 v73, v73
	v_exp_f32_e32 v72, v105
	v_exp_f32_e32 v152, v57
	v_add_f32_e32 v48, v68, v48
	v_add_f32_e32 v49, v69, v49
	v_add_f32_e32 v50, v84, v50
	v_add_f32_e32 v51, v85, v51
	v_exp_f32_e32 v169, v90
	v_exp_f32_e32 v89, v74
	v_exp_f32_e32 v88, v106
	v_exp_f32_e32 v168, v58
	v_add_f32_e32 v48, v148, v48
	v_add_f32_e32 v49, v149, v49
	v_add_f32_e32 v50, v100, v50
	v_add_f32_e32 v51, v101, v51
	v_exp_f32_e32 v171, v91
	v_exp_f32_e32 v75, v75
	v_exp_f32_e32 v74, v107
	v_exp_f32_e32 v170, v59
	v_add_f32_e32 v48, v70, v48
	v_add_f32_e32 v49, v71, v49
	v_add_f32_e32 v50, v86, v50
	v_add_f32_e32 v51, v87, v51
	v_exp_f32_e32 v173, v92
	v_exp_f32_e32 v91, v76
	v_exp_f32_e32 v90, v108
	v_exp_f32_e32 v172, v60
	v_add_f32_e32 v48, v102, v48
	v_add_f32_e32 v49, v103, v49
	v_add_f32_e32 v50, v150, v50
	v_add_f32_e32 v51, v151, v51
	v_exp_f32_e32 v175, v93
	v_exp_f32_e32 v77, v77
	v_exp_f32_e32 v76, v109
	v_exp_f32_e32 v174, v61
	v_add_f32_e32 v48, v72, v48
	v_add_f32_e32 v49, v73, v49
	v_add_f32_e32 v50, v152, v50
	v_add_f32_e32 v51, v153, v51
	v_exp_f32_e32 v177, v94
	v_exp_f32_e32 v93, v78
	v_exp_f32_e32 v92, v110
	v_exp_f32_e32 v176, v62
	v_add_f32_e32 v48, v88, v48
	v_add_f32_e32 v49, v89, v49
	v_add_f32_e32 v50, v168, v50
	v_add_f32_e32 v51, v169, v51
	v_exp_f32_e32 v179, v95
	v_exp_f32_e32 v79, v79
	v_exp_f32_e32 v78, v111
	v_exp_f32_e32 v178, v63
	v_add_f32_e32 v48, v74, v48
	v_add_f32_e32 v49, v75, v49
	v_add_f32_e32 v50, v170, v50
	v_add_f32_e32 v51, v171, v51
	v_add_f32_e32 v48, v90, v48
	v_add_f32_e32 v49, v91, v49
	v_add_f32_e32 v50, v172, v50
	v_add_f32_e32 v51, v173, v51
	v_add_f32_e32 v48, v76, v48
	v_add_f32_e32 v49, v77, v49
	v_add_f32_e32 v50, v174, v50
	v_add_f32_e32 v51, v175, v51
	v_add_f32_e32 v48, v92, v48
	v_add_f32_e32 v49, v93, v49
	v_add_f32_e32 v50, v176, v50
	v_add_f32_e32 v51, v177, v51
	v_add_f32_e32 v48, v78, v48
	v_add_f32_e32 v49, v79, v49
	v_add_f32_e32 v50, v178, v50
	v_add_f32_e32 v51, v179, v51
	v_cvt_pk_bf16_f32 v57, v145, v67
	v_add_f32_e32 v48, v50, v48
	v_add_f32_e32 v49, v51, v49
	v_cvt_pk_bf16_f32 v67, v148, v70
	v_cvt_pk_bf16_f32 v70, v90, v76
	v_add3_u32 v76, s94, v161, v163
	v_add_f32_e32 v48, v48, v49
	v_cvt_pk_bf16_f32 v56, v143, v65
	v_cvt_pk_bf16_f32 v65, v144, v66
	v_cvt_pk_bf16_f32 v66, v146, v68
	v_cvt_pk_bf16_f32 v68, v102, v72
	v_cvt_pk_bf16_f32 v72, v140, v80
	v_add3_u32 v140, v76, v165, v157
	v_add_f32_e32 v162, v162, v48
	v_cvt_pk_bf16_f32 v48, v141, v81
	v_cvt_pk_bf16_f32 v49, v97, v83
	v_cvt_pk_bf16_f32 v50, v99, v85
	v_cvt_pk_bf16_f32 v51, v101, v87
	v_cvt_pk_bf16_f32 v58, v147, v69
	v_cvt_pk_bf16_f32 v59, v149, v71
	v_cvt_pk_bf16_f32 v60, v103, v73
	v_cvt_pk_bf16_f32 v61, v89, v75
	v_cvt_pk_bf16_f32 v62, v91, v77
	v_cvt_pk_bf16_f32 v63, v93, v79
	v_cvt_pk_bf16_f32 v69, v88, v74
	v_cvt_pk_bf16_f32 v71, v92, v78
	v_cvt_pk_bf16_f32 v73, v96, v82
	v_cvt_pk_bf16_f32 v74, v98, v84
	v_cvt_pk_bf16_f32 v75, v100, v86
	s_waitcnt vmcnt(0)
; #define LAS __attribute__((address_space(3)))
; __device__ __forceinline__ s16x4 vtr(const LAS unsigned char* p) { return __builtin_bit_cast(s16x4, __builtin_amdgcn_ds_read_tr16_b64_v4i16((LAS v4i16_t*)p)); }
; __device__ __forceinline__ void softmax_pv2(f32x16& a0, f32x16& a1, f32x16& b0, f32x16& b1, f32x16 (&o)[2], float& mref, float& l, f32x16& cn, bool first, LAS float* wsf, ...
;     ...
;     const int voff = (4 * hi + ((lane & 15) >> 2)) * 64 + ((lane >> 4) & 1) * 32 + (lane & 3) * 8;
; #pragma unroll
;     for (int t = 0; t < 2; ++t) { const LAS unsigned char* vb = (t == 0 ? VsA : VsB) + voff;
;         s16x4 lo[8], hh[8];
; #pragma unroll
;         for (int db = 0; db < 2; ++db)
; #pragma unroll
;             for (int ks = 0; ks < 4; ++ks) { lo[db * 4 + ks] = vtr(vb + db * 4096 + ks * 1024); hh[db * 4 + ks] = vtr(vb + db * 4096 + ks * 1024 + 512); }
;         __builtin_amdgcn_sched_barrier(0);
;     #pragma unroll
;         for (int ks = 0; ks < 4; ++ks)
; #pragma unroll
;             for (int db = 0; db < 2; ++db) { const int i = db * 4 + ks;
;                 const bf16x8 vf = (bf16x8){lo[i][0], lo[i][1], lo[i][2], lo[i][3], hh[i][0], hh[i][1], hh[i][2], hh[i][3]};
;                 o[db] = __builtin_amdgcn_mfma_f32_32x32x16_bf16(pa[4 * t + ks], vf, o[db], 0, 0, 0); }
;         }
	ds_read_b64_tr_b16 v[76:77], v140 offset:8192
	ds_read_b64_tr_b16 v[78:79], v140 offset:8704
	ds_read_b64_tr_b16 v[80:81], v140 offset:9216
	ds_read_b64_tr_b16 v[82:83], v140 offset:9728
	ds_read_b64_tr_b16 v[84:85], v140 offset:10240
	ds_read_b64_tr_b16 v[86:87], v140 offset:10752
	ds_read_b64_tr_b16 v[88:89], v140 offset:11264
	ds_read_b64_tr_b16 v[90:91], v140 offset:11776
	ds_read_b64_tr_b16 v[92:93], v140 offset:12288
	ds_read_b64_tr_b16 v[94:95], v140 offset:12800
	ds_read_b64_tr_b16 v[96:97], v140 offset:13312
	ds_read_b64_tr_b16 v[98:99], v140 offset:13824
	ds_read_b64_tr_b16 v[100:101], v140 offset:14336
	ds_read_b64_tr_b16 v[102:103], v140 offset:14848
	ds_read_b64_tr_b16 v[104:105], v140 offset:15360
	ds_read_b64_tr_b16 v[106:107], v140 offset:15872
	v_cvt_pk_bf16_f32 v52, v151, v153
	v_cvt_pk_bf16_f32 v53, v169, v171
	v_cvt_pk_bf16_f32 v54, v173, v175
	v_cvt_pk_bf16_f32 v55, v177, v179
	v_cvt_pk_bf16_f32 v64, v142, v64
	v_cvt_pk_bf16_f32 v108, v150, v152
	v_cvt_pk_bf16_f32 v109, v168, v170
	v_cvt_pk_bf16_f32 v110, v172, v174
	v_cvt_pk_bf16_f32 v111, v176, v178
	s_waitcnt lgkmcnt(14)
	v_mfma_f32_32x32x16_bf16 v[16:31], v[48:51], v[76:79], v[16:31]
	s_waitcnt lgkmcnt(6)
	v_mfma_f32_32x32x16_bf16 v[0:15], v[48:51], v[92:95], v[0:15]
	v_mfma_f32_32x32x16_bf16 v[16:31], v[52:55], v[80:83], v[16:31]
	s_waitcnt lgkmcnt(4)
	v_mfma_f32_32x32x16_bf16 v[0:15], v[52:55], v[96:99], v[0:15]
	v_mfma_f32_32x32x16_bf16 v[16:31], v[56:59], v[84:87], v[16:31]
	s_waitcnt lgkmcnt(2)
	v_mfma_f32_32x32x16_bf16 v[0:15], v[56:59], v[100:103], v[0:15]
	ds_read_b64_tr_b16 v[48:49], v140 offset:24576
	ds_read_b64_tr_b16 v[50:51], v140 offset:25088
	ds_read_b64_tr_b16 v[52:53], v140 offset:25600
	ds_read_b64_tr_b16 v[54:55], v140 offset:26112
	ds_read_b64_tr_b16 v[56:57], v140 offset:26624
	ds_read_b64_tr_b16 v[58:59], v140 offset:27136
	ds_read_b64_tr_b16 v[76:77], v140 offset:27648
	ds_read_b64_tr_b16 v[78:79], v140 offset:28160
	v_mfma_f32_32x32x16_bf16 v[16:31], v[60:63], v[88:91], v[16:31]
	ds_read_b64_tr_b16 v[80:81], v140 offset:28672
	ds_read_b64_tr_b16 v[82:83], v140 offset:29184
	ds_read_b64_tr_b16 v[84:85], v140 offset:29696
	ds_read_b64_tr_b16 v[86:87], v140 offset:30208
	ds_read_b64_tr_b16 v[88:89], v140 offset:30720
	ds_read_b64_tr_b16 v[90:91], v140 offset:31232
	ds_read_b64_tr_b16 v[92:93], v140 offset:31744
	ds_read_b64_tr_b16 v[94:95], v140 offset:32256
	s_waitcnt lgkmcnt(14)
	v_mfma_f32_32x32x16_bf16 v[0:15], v[60:63], v[104:107], v[0:15]
	v_mfma_f32_32x32x16_bf16 v[16:31], v[64:67], v[48:51], v[16:31]
	s_waitcnt lgkmcnt(6)
	v_mfma_f32_32x32x16_bf16 v[0:15], v[64:67], v[80:83], v[0:15]
	v_mfma_f32_32x32x16_bf16 v[16:31], v[68:71], v[52:55], v[16:31]
	s_waitcnt lgkmcnt(4)
	v_mfma_f32_32x32x16_bf16 v[0:15], v[68:71], v[84:87], v[0:15]
	v_mfma_f32_32x32x16_bf16 v[16:31], v[72:75], v[56:59], v[16:31]
	s_waitcnt lgkmcnt(2)
	v_mfma_f32_32x32x16_bf16 v[0:15], v[72:75], v[88:91], v[0:15]
	v_mfma_f32_32x32x16_bf16 v[16:31], v[108:111], v[76:79], v[16:31]
	s_waitcnt lgkmcnt(0)
	v_mfma_f32_32x32x16_bf16 v[0:15], v[108:111], v[92:95], v[0:15]

; #define LAS __attribute__((address_space(3)))
; __device__ __forceinline__ void moba_unit(const MobaArgs& A, int b, int h, int qb, LAS unsigned char* lds, int wave, bool tables) {
;     ...
;             if (near) {
;                 const LAS float* lp = lut + (LUTA_TOP - qpos + kt0 + 4 * hi);
; #pragma unroll
;                 for (int r = 0; r < 16; ++r) { const int c = (r & 3) + 8 * (r >> 2); a0[r] += lp[c]; a1[r] += lp[c + 32]; b0[r] += lp[c + 64]; b1[r] += lp[c + 96]; }
;                 if (own && kt0 + 127 > qmin) {
;                     const int lim = qpos - kt0 - 4 * hi;
; #pragma unroll
;                     for (int r = 0; r < 16; ++r) { const int c = (r & 3) + 8 * (r >> 2); if (c > lim) a0[r] = NEG; if (c + 32 > lim) a1[r] = NEG; if (c + 64 > lim) b0[r] = NEG; if (c + 96 > lim) b1[r] = NEG; }
.LBB0_667:
	s_andn2_b64 vcc, exec, s[10:11]
	s_cbranch_vccnz .LBB0_670
	v_sub_u32_e32 v140, s16, v134
	v_lshl_add_u32 v167, v140, 2, v166
	v_add_u32_e32 v167, 0x10fc, v167
	ds_read2_b32 v[168:169], v167 offset1:1
	ds_read2_b32 v[170:171], v167 offset0:32 offset1:33
	ds_read2_b32 v[172:173], v167 offset0:64 offset1:65
	ds_read2_b32 v[140:141], v167 offset0:96 offset1:97
	ds_read2_b32 v[174:175], v167 offset0:2 offset1:3
	ds_read2_b32 v[176:177], v167 offset0:34 offset1:35
	ds_read2_b32 v[178:179], v167 offset0:66 offset1:67
	ds_read2_b32 v[142:143], v167 offset0:98 offset1:99
	ds_read2_b32 v[180:181], v167 offset0:8 offset1:9
	ds_read2_b32 v[182:183], v167 offset0:40 offset1:41
	ds_read2_b32 v[184:185], v167 offset0:72 offset1:73
	ds_read2_b32 v[144:145], v167 offset0:104 offset1:105
	ds_read2_b32 v[186:187], v167 offset0:10 offset1:11
	ds_read2_b32 v[188:189], v167 offset0:42 offset1:43
	ds_read2_b32 v[190:191], v167 offset0:74 offset1:75
	ds_read2_b32 v[146:147], v167 offset0:106 offset1:107
	ds_read2_b32 v[192:193], v167 offset0:16 offset1:17
	ds_read2_b32 v[194:195], v167 offset0:48 offset1:49
	ds_read2_b32 v[196:197], v167 offset0:80 offset1:81
	ds_read2_b32 v[148:149], v167 offset0:112 offset1:113
	ds_read2_b32 v[198:199], v167 offset0:18 offset1:19
	ds_read2_b32 v[200:201], v167 offset0:50 offset1:51
	ds_read2_b32 v[202:203], v167 offset0:82 offset1:83
	ds_read2_b32 v[150:151], v167 offset0:114 offset1:115
	ds_read2_b32 v[204:205], v167 offset0:24 offset1:25
	ds_read2_b32 v[206:207], v167 offset0:56 offset1:57
	ds_read2_b32 v[208:209], v167 offset0:88 offset1:89
	ds_read2_b32 v[152:153], v167 offset0:120 offset1:121
	ds_read2_b32 v[210:211], v167 offset0:26 offset1:27
	s_waitcnt lgkmcnt(0)
	v_add_f32_e32 v80, v80, v168
	v_add_f32_e32 v81, v81, v169
	ds_read2_b32 v[168:169], v167 offset0:58 offset1:59
	s_cmp_ge_i32 s96, s17
	s_cselect_b64 s[6:7], -1, 0
	s_waitcnt lgkmcnt(0)
	v_add_f32_e32 v78, v78, v168
	v_add_f32_e32 v79, v79, v169
	ds_read2_b32 v[168:169], v167 offset0:90 offset1:91
	s_xor_b64 s[8:9], s[8:9], -1
	s_or_b64 s[6:7], s[8:9], s[6:7]
	v_add_f32_e32 v92, v92, v204
	v_add_f32_e32 v93, v93, v205
	v_add_f32_e32 v90, v90, v198
	v_add_f32_e32 v91, v91, v199
	s_waitcnt lgkmcnt(0)
	v_add_f32_e32 v110, v110, v168
	v_add_f32_e32 v111, v111, v169
	ds_read2_b32 v[168:169], v167 offset0:122 offset1:123
	v_add_f32_e32 v94, v94, v210
	v_add_f32_e32 v95, v95, v211
	v_add_f32_e32 v88, v88, v192
	v_add_f32_e32 v89, v89, v193
	v_add_f32_e32 v86, v86, v186
	v_add_f32_e32 v87, v87, v187
	v_add_f32_e32 v84, v84, v180
	v_add_f32_e32 v85, v85, v181
	v_add_f32_e32 v82, v82, v174
	v_add_f32_e32 v83, v83, v175
	v_add_f32_e32 v76, v76, v206
	v_add_f32_e32 v77, v77, v207
	v_add_f32_e32 v74, v74, v200
	v_add_f32_e32 v75, v75, v201
	v_add_f32_e32 v72, v72, v194
	v_add_f32_e32 v73, v73, v195
	v_add_f32_e32 v70, v70, v188
	v_add_f32_e32 v71, v71, v189
	v_add_f32_e32 v68, v68, v182
	v_add_f32_e32 v69, v69, v183
	v_add_f32_e32 v66, v66, v176
	v_add_f32_e32 v67, v67, v177
	v_add_f32_e32 v64, v64, v170
	v_add_f32_e32 v65, v65, v171
	v_add_f32_e32 v108, v108, v208
	v_add_f32_e32 v109, v109, v209
	v_add_f32_e32 v106, v106, v202
	v_add_f32_e32 v107, v107, v203
	v_add_f32_e32 v104, v104, v196
	v_add_f32_e32 v105, v105, v197
	v_add_f32_e32 v102, v102, v190
	v_add_f32_e32 v103, v103, v191
	v_add_f32_e32 v100, v100, v184
	v_add_f32_e32 v101, v101, v185
	v_add_f32_e32 v98, v98, v178
	v_add_f32_e32 v99, v99, v179
	v_add_f32_e32 v96, v96, v172
	v_add_f32_e32 v97, v97, v173
	s_waitcnt lgkmcnt(0)
	v_add_f32_e32 v62, v62, v168
	v_add_f32_e32 v63, v63, v169
	v_add_f32_e32 v60, v60, v152
	v_add_f32_e32 v61, v61, v153
	v_add_f32_e32 v58, v58, v150
	v_add_f32_e32 v59, v59, v151
	v_add_f32_e32 v56, v56, v148
	v_add_f32_e32 v57, v57, v149
	v_add_f32_e32 v54, v54, v146
	v_add_f32_e32 v55, v55, v147
	v_add_f32_e32 v52, v52, v144
	v_add_f32_e32 v53, v53, v145
	v_add_f32_e32 v50, v50, v142
	v_add_f32_e32 v51, v51, v143
	v_add_f32_e32 v48, v48, v140
	v_add_f32_e32 v49, v49, v141
	s_and_b64 vcc, exec, s[6:7]
	s_cbranch_vccnz .LBB0_670
	v_add_u32_e32 v140, s16, v160
	v_sub_u32_e32 v140, v134, v140
	v_cmp_gt_i32_e64 s[44:45], 26, v140
	v_cmp_gt_i32_e64 s[60:61], 27, v140
	s_and_b64 s[44:45], s[60:61], s[44:45]
	v_cndmask_b32_e64 v94, v94, v252, s[44:45]
	v_cndmask_b32_e64 v95, v95, v252, s[60:61]
	v_cmp_gt_i32_e64 s[60:61], 25, v140
	s_and_b64 s[44:45], s[44:45], s[60:61]
	v_cmp_gt_i32_e64 s[60:61], 24, v140
	v_cndmask_b32_e64 v93, v93, v252, s[44:45]
	s_and_b64 s[44:45], s[44:45], s[60:61]
	v_cmp_gt_i32_e64 s[60:61], 19, v140
	v_cndmask_b32_e64 v92, v92, v252, s[44:45]
	s_and_b64 s[44:45], s[44:45], s[60:61]
	v_cmp_gt_i32_e64 s[60:61], 18, v140
	v_cndmask_b32_e64 v91, v91, v252, s[44:45]
	s_and_b64 s[44:45], s[44:45], s[60:61]
	v_cmp_gt_i32_e64 s[60:61], 17, v140
	v_cndmask_b32_e64 v90, v90, v252, s[44:45]
	s_and_b64 s[44:45], s[44:45], s[60:61]
	v_cmp_gt_i32_e64 s[60:61], 16, v140
	v_cndmask_b32_e64 v89, v89, v252, s[44:45]
	s_and_b64 s[44:45], s[44:45], s[60:61]
	v_cmp_gt_i32_e64 s[60:61], 11, v140
	v_cmp_gt_i32_e64 s[28:29], 10, v140
	s_and_b64 s[60:61], s[44:45], s[60:61]
	v_cmp_gt_i32_e64 s[58:59], 9, v140
	v_cndmask_b32_e64 v87, v87, v252, s[60:61]
	s_and_b64 s[60:61], s[60:61], s[28:29]
	v_cmp_gt_i32_e64 s[50:51], 8, v140
	v_cndmask_b32_e64 v86, v86, v252, s[60:61]
	s_and_b64 s[60:61], s[60:61], s[58:59]
	v_cmp_gt_i32_e64 s[36:37], 3, v140
	v_cndmask_b32_e64 v85, v85, v252, s[60:61]
	s_and_b64 s[60:61], s[60:61], s[50:51]
	v_cmp_gt_i32_e64 s[56:57], 2, v140
	v_cndmask_b32_e64 v84, v84, v252, s[60:61]
	s_and_b64 s[60:61], s[60:61], s[36:37]
	v_cmp_gt_i32_e64 s[52:53], 1, v140
; __device__ __forceinline__ void moba_unit(const MobaArgs& A, int b, int h, int qb, LAS unsigned char* lds, int wave, bool tables) {
;     ...
;                 if (own && kt0 + 127 > qmin) {
;                     const int lim = qpos - kt0 - 4 * hi;
; #pragma unroll
;                     for (int r = 0; r < 16; ++r) { const int c = (r & 3) + 8 * (r >> 2); if (c > lim) a0[r] = NEG; if (c + 32 > lim) a1[r] = NEG; if (c + 64 > lim) b0[r] = NEG; if (c + 96 > lim) b1[r] = NEG; }
;                 }
	v_cndmask_b32_e64 v83, v83, v252, s[60:61]
	s_and_b64 s[60:61], s[60:61], s[56:57]
	v_cmp_gt_i32_e64 s[54:55], 0, v140
	v_cndmask_b32_e64 v82, v82, v252, s[60:61]
	s_and_b64 s[60:61], s[60:61], s[52:53]
	s_and_b64 s[54:55], s[60:61], s[54:55]
	v_cndmask_b32_e64 v81, v81, v252, s[60:61]
	v_cmp_gt_i32_e64 s[60:61], 58, v140
	v_cndmask_b32_e64 v80, v80, v252, s[54:55]
	v_cmp_gt_i32_e64 s[54:55], 59, v140
	v_cmp_gt_i32_e64 s[56:57], 48, v140
	v_cmp_gt_i32_e64 s[58:59], 43, v140
	v_cndmask_b32_e64 v79, v79, v252, s[54:55]
	s_and_b64 s[54:55], s[54:55], s[60:61]
	v_cmp_gt_i32_e64 s[60:61], 57, v140
	v_cndmask_b32_e64 v78, v78, v252, s[54:55]
	s_and_b64 s[54:55], s[54:55], s[60:61]
	v_cmp_gt_i32_e64 s[60:61], 56, v140
	v_cndmask_b32_e64 v77, v77, v252, s[54:55]
	s_and_b64 s[54:55], s[54:55], s[60:61]
	v_cmp_gt_i32_e64 s[60:61], 51, v140
	v_cndmask_b32_e64 v76, v76, v252, s[54:55]
	s_and_b64 s[54:55], s[54:55], s[60:61]
	v_cmp_gt_i32_e64 s[60:61], 50, v140
	v_cndmask_b32_e64 v75, v75, v252, s[54:55]
	s_and_b64 s[54:55], s[54:55], s[60:61]
	v_cmp_gt_i32_e64 s[60:61], 49, v140
	s_and_b64 s[60:61], s[54:55], s[60:61]
	s_and_b64 s[56:57], s[60:61], s[56:57]
	v_cmp_gt_i32_e64 s[48:49], 42, v140
	s_and_b64 s[58:59], s[56:57], s[58:59]
	v_cmp_gt_i32_e64 s[46:47], 41, v140
	v_cndmask_b32_e64 v71, v71, v252, s[58:59]
	s_and_b64 s[58:59], s[58:59], s[48:49]
	v_cmp_gt_i32_e64 s[42:43], 40, v140
	v_cndmask_b32_e64 v70, v70, v252, s[58:59]
	s_and_b64 s[58:59], s[58:59], s[46:47]
	v_cmp_gt_i32_e64 s[40:41], 35, v140
	v_cndmask_b32_e64 v69, v69, v252, s[58:59]
	s_and_b64 s[58:59], s[58:59], s[42:43]
	v_cmp_gt_i32_e64 s[38:39], 34, v140
	v_cndmask_b32_e64 v68, v68, v252, s[58:59]
	s_and_b64 s[58:59], s[58:59], s[40:41]
	v_cmp_gt_i32_e64 s[34:35], 33, v140
	s_and_b64 s[38:39], s[58:59], s[38:39]
	v_cmp_gt_i32_e64 s[30:31], 32, v140
	v_cndmask_b32_e64 v66, v66, v252, s[38:39]
	s_and_b64 s[38:39], s[38:39], s[34:35]
	s_and_b64 s[30:31], s[38:39], s[30:31]
	v_cndmask_b32_e64 v65, v65, v252, s[38:39]
	s_movk_i32 s38, 0x5a
	v_cndmask_b32_e64 v64, v64, v252, s[30:31]
	s_movk_i32 s30, 0x5b
	v_cmp_gt_i32_e64 s[38:39], s38, v140
	v_cmp_gt_i32_e64 s[30:31], s30, v140
	v_cndmask_b32_e64 v67, v67, v252, s[58:59]
	s_movk_i32 s58, 0x58
	v_cndmask_b32_e64 v111, v111, v252, s[30:31]
	s_and_b64 s[30:31], s[30:31], s[38:39]
	s_movk_i32 s38, 0x59
	v_cmp_gt_i32_e64 s[38:39], s38, v140
	s_movk_i32 s42, 0x53
	v_cmp_gt_i32_e64 s[58:59], s58, v140
	v_cndmask_b32_e64 v110, v110, v252, s[30:31]
	s_and_b64 s[30:31], s[30:31], s[38:39]
	s_movk_i32 s48, 0x52
	v_cmp_gt_i32_e64 s[42:43], s42, v140
	v_cndmask_b32_e64 v109, v109, v252, s[30:31]
	s_and_b64 s[30:31], s[30:31], s[58:59]
	v_cndmask_b32_e64 v73, v73, v252, s[60:61]
	s_movk_i32 s60, 0x51
	v_cmp_gt_i32_e64 s[48:49], s48, v140
	v_cndmask_b32_e64 v108, v108, v252, s[30:31]
	s_and_b64 s[30:31], s[30:31], s[42:43]
	s_movk_i32 s52, 0x50
	v_cmp_gt_i32_e64 s[60:61], s60, v140
	v_cndmask_b32_e64 v107, v107, v252, s[30:31]
	s_and_b64 s[30:31], s[30:31], s[48:49]
	s_movk_i32 s50, 0x4b
	v_cmp_gt_i32_e64 s[52:53], s52, v140
	v_cndmask_b32_e64 v106, v106, v252, s[30:31]
	s_and_b64 s[30:31], s[30:31], s[60:61]
	v_cndmask_b32_e64 v88, v88, v252, s[44:45]
	s_movk_i32 s44, 0x4a
	v_cmp_gt_i32_e64 s[50:51], s50, v140
	v_cndmask_b32_e64 v105, v105, v252, s[30:31]
	s_and_b64 s[30:31], s[30:31], s[52:53]
	s_movk_i32 s14, 0x49
	v_cmp_gt_i32_e64 s[44:45], s44, v140
	v_cndmask_b32_e64 v104, v104, v252, s[30:31]
	s_and_b64 s[30:31], s[30:31], s[50:51]
	s_movk_i32 s12, 0x48
	v_cmp_gt_i32_e64 s[26:27], s14, v140
	v_cndmask_b32_e64 v103, v103, v252, s[30:31]
	s_and_b64 s[30:31], s[30:31], s[44:45]
	s_movk_i32 s10, 0x43
	v_cmp_gt_i32_e64 s[24:25], s12, v140
	s_and_b64 s[26:27], s[30:31], s[26:27]
	s_movk_i32 s6, 0x60
	s_movk_i32 s8, 0x42
	v_cmp_gt_i32_e64 s[22:23], s10, v140
	s_and_b64 s[24:25], s[26:27], s[24:25]
	v_cmp_gt_i32_e32 vcc, s6, v140
	s_movk_i32 s6, 0x41
	v_cmp_gt_i32_e64 s[20:21], s8, v140
	s_and_b64 s[22:23], s[24:25], s[22:23]
	v_cmp_gt_i32_e64 s[18:19], s6, v140
	s_and_b64 s[20:21], s[22:23], s[20:21]
	v_cmp_gt_i32_e64 s[16:17], 64, v140
	s_and_b64 s[18:19], s[20:21], s[18:19]
	s_and_b64 s[16:17], s[18:19], s[16:17]
	s_movk_i32 s58, 0x7a
	v_cndmask_b32_e64 v96, v96, v252, s[16:17]
	s_movk_i32 s16, 0x7b
	s_movk_i32 s38, 0x79
	v_cmp_gt_i32_e64 s[58:59], s58, v140
	v_cmp_gt_i32_e64 s[16:17], s16, v140
	s_movk_i32 s34, 0x78
	v_cmp_gt_i32_e64 s[38:39], s38, v140
	v_cndmask_b32_e64 v63, v63, v252, s[16:17]
	s_and_b64 s[16:17], s[16:17], s[58:59]
	s_movk_i32 s40, 0x73
	v_cmp_gt_i32_e64 s[34:35], s34, v140
	v_cndmask_b32_e64 v62, v62, v252, s[16:17]
	s_and_b64 s[16:17], s[16:17], s[38:39]
	s_movk_i32 s46, 0x72
	v_cmp_gt_i32_e64 s[40:41], s40, v140
	v_cndmask_b32_e64 v61, v61, v252, s[16:17]
	s_and_b64 s[16:17], s[16:17], s[34:35]
	v_cndmask_b32_e64 v72, v72, v252, s[56:57]
	s_movk_i32 s56, 0x71
	v_cmp_gt_i32_e64 s[46:47], s46, v140
	v_cndmask_b32_e64 v60, v60, v252, s[16:17]
	s_and_b64 s[16:17], s[16:17], s[40:41]
	v_cndmask_b32_e64 v74, v74, v252, s[54:55]
	s_movk_i32 s54, 0x70
	v_cmp_gt_i32_e64 s[56:57], s56, v140
	v_cndmask_b32_e64 v59, v59, v252, s[16:17]
	s_and_b64 s[16:17], s[16:17], s[46:47]
	s_movk_i32 s36, 0x6b
	v_cmp_gt_i32_e64 s[54:55], s54, v140
	v_cndmask_b32_e64 v58, v58, v252, s[16:17]
	s_and_b64 s[16:17], s[16:17], s[56:57]
	s_movk_i32 s28, 0x6a
	v_cmp_gt_i32_e64 s[36:37], s36, v140
	v_cndmask_b32_e64 v57, v57, v252, s[16:17]
	s_and_b64 s[16:17], s[16:17], s[54:55]
	s_movk_i32 s14, 0x69
	v_cmp_gt_i32_e64 s[28:29], s28, v140
	v_cndmask_b32_e64 v56, v56, v252, s[16:17]
	s_and_b64 s[16:17], s[16:17], s[36:37]
	s_movk_i32 s12, 0x68
	v_cmp_gt_i32_e64 s[14:15], s14, v140
	v_cndmask_b32_e64 v55, v55, v252, s[16:17]
	s_and_b64 s[16:17], s[16:17], s[28:29]
	s_movk_i32 s10, 0x63
	v_cmp_gt_i32_e64 s[12:13], s12, v140
	s_and_b64 s[14:15], s[16:17], s[14:15]
	s_movk_i32 s8, 0x62
	v_cmp_gt_i32_e64 s[10:11], s10, v140
	s_and_b64 s[12:13], s[14:15], s[12:13]
	s_movk_i32 s6, 0x61
	v_cmp_gt_i32_e64 s[8:9], s8, v140
	s_and_b64 s[10:11], s[12:13], s[10:11]
	v_cmp_gt_i32_e64 s[6:7], s6, v140
	s_and_b64 s[8:9], s[10:11], s[8:9]
	s_and_b64 s[6:7], s[8:9], s[6:7]
	s_and_b64 vcc, s[6:7], vcc
	s_mov_b32 s61, 0xe000
	s_mov_b32 s60, 0xc000
	v_cndmask_b32_e64 v102, v102, v252, s[30:31]
	v_cndmask_b32_e64 v101, v101, v252, s[26:27]
	v_cndmask_b32_e64 v100, v100, v252, s[24:25]
	v_cndmask_b32_e64 v99, v99, v252, s[22:23]
	v_cndmask_b32_e64 v98, v98, v252, s[20:21]
	v_cndmask_b32_e64 v97, v97, v252, s[18:19]
	v_cndmask_b32_e64 v54, v54, v252, s[16:17]
	v_cndmask_b32_e64 v53, v53, v252, s[14:15]
	v_cndmask_b32_e64 v52, v52, v252, s[12:13]
	v_cndmask_b32_e64 v51, v51, v252, s[10:11]
	v_cndmask_b32_e64 v50, v50, v252, s[8:9]
	v_cndmask_b32_e64 v49, v49, v252, s[6:7]
	v_cndmask_b32_e32 v48, v48, v252, vcc

; __device__ __forceinline__ float fast_exp2(float x) { return __builtin_amdgcn_exp2f(x); }
; #define PK8(P, B) __builtin_bit_cast(bf16x8, (u32x4){pk_bf16(P[B], P[B + 1]), pk_bf16(P[B + 2], P[B + 3]), pk_bf16(P[B + 4], P[B + 5]), pk_bf16(P[B + 6], P[B + 7])})
; __device__ __forceinline__ void softmax_pv2(f32x16& a0, f32x16& a1, f32x16& b0, f32x16& b1, f32x16 (&o)[2], float& mref, float& l, f32x16& cn, bool first, LAS float* wsf, ...
;     ...
;     float s0 = 0.f, s1 = 0.f, s2 = 0.f, s3 = 0.f;
; #pragma unroll
;     for (int r = 0; r < 16; ++r) { a0[r] = fast_exp2(a0[r]); a1[r] = fast_exp2(a1[r]); b0[r] = fast_exp2(b0[r]); b1[r] = fast_exp2(b1[r]); s0 += a0[r]; s1 += a1[r]; s2 += b0[r]; s3 += b1[r]; }
;     l += (s0 + s1) + (s2 + s3);
;     bf16x8 pa[8];
;     ...
;     pa[0] = PK8(a0, 0); pa[1] = PK8(a0, 8); pa[2] = PK8(a1, 0); pa[3] = PK8(a1, 8); pa[4] = PK8(b0, 0); pa[5] = PK8(b0, 8); pa[6] = PK8(b1, 0); pa[7] = PK8(b1, 8);
.LBB0_724:
	v_exp_f32_e32 v139, v80
	v_exp_f32_e32 v141, v64
	v_exp_f32_e32 v140, v96
	v_exp_f32_e32 v138, v48
	v_exp_f32_e32 v81, v81
	v_exp_f32_e32 v65, v65
	v_exp_f32_e32 v64, v97
	v_exp_f32_e32 v80, v49
	v_exp_f32_e32 v97, v82
	v_exp_f32_e32 v143, v66
	v_exp_f32_e32 v142, v98
	v_exp_f32_e32 v96, v50
	v_exp_f32_e32 v83, v83
	v_exp_f32_e32 v67, v67
	v_exp_f32_e32 v66, v99
	v_exp_f32_e32 v82, v51
	v_exp_f32_e32 v99, v84
	v_exp_f32_e32 v145, v68
	v_exp_f32_e32 v144, v100
	v_exp_f32_e32 v98, v52
	v_add_f32_e32 v48, 0, v140
	v_add_f32_e32 v49, 0, v141
	v_add_f32_e32 v50, 0, v138
	v_add_f32_e32 v51, 0, v139
	v_add_f32_e32 v48, v64, v48
	v_add_f32_e32 v49, v65, v49
	v_add_f32_e32 v50, v80, v50
	v_add_f32_e32 v51, v81, v51
	v_exp_f32_e32 v85, v85
	v_exp_f32_e32 v69, v69
	v_exp_f32_e32 v68, v101
	v_exp_f32_e32 v84, v53
	v_add_f32_e32 v48, v142, v48
	v_add_f32_e32 v49, v143, v49
	v_add_f32_e32 v50, v96, v50
	v_add_f32_e32 v51, v97, v51
	v_exp_f32_e32 v101, v86
	v_exp_f32_e32 v147, v70
	v_exp_f32_e32 v146, v102
	v_exp_f32_e32 v100, v54
	v_add_f32_e32 v48, v66, v48
	v_add_f32_e32 v49, v67, v49
	v_add_f32_e32 v50, v82, v50
	v_add_f32_e32 v51, v83, v51
	v_exp_f32_e32 v87, v87
	v_exp_f32_e32 v71, v71
	v_exp_f32_e32 v70, v103
	v_exp_f32_e32 v86, v55
	v_add_f32_e32 v48, v144, v48
	v_add_f32_e32 v49, v145, v49
	v_add_f32_e32 v50, v98, v50
	v_add_f32_e32 v51, v99, v51
	v_exp_f32_e32 v149, v88
	v_exp_f32_e32 v103, v72
	v_exp_f32_e32 v102, v104
	v_exp_f32_e32 v148, v56
	v_exp_f32_e32 v151, v89
	v_exp_f32_e32 v73, v73
	v_exp_f32_e32 v72, v105
	v_exp_f32_e32 v150, v57
	v_add_f32_e32 v48, v68, v48
	v_add_f32_e32 v49, v69, v49
	v_add_f32_e32 v50, v84, v50
	v_add_f32_e32 v51, v85, v51
	v_exp_f32_e32 v169, v90
	v_exp_f32_e32 v89, v74
	v_exp_f32_e32 v88, v106
	v_exp_f32_e32 v168, v58
	v_add_f32_e32 v48, v146, v48
	v_add_f32_e32 v49, v147, v49
	v_add_f32_e32 v50, v100, v50
	v_add_f32_e32 v51, v101, v51
	v_exp_f32_e32 v171, v91
	v_exp_f32_e32 v75, v75
	v_exp_f32_e32 v74, v107
	v_exp_f32_e32 v170, v59
	v_add_f32_e32 v48, v70, v48
	v_add_f32_e32 v49, v71, v49
	v_add_f32_e32 v50, v86, v50
	v_add_f32_e32 v51, v87, v51
	v_exp_f32_e32 v173, v92
	v_exp_f32_e32 v91, v76
	v_exp_f32_e32 v90, v108
	v_exp_f32_e32 v172, v60
	v_add_f32_e32 v48, v102, v48
	v_add_f32_e32 v49, v103, v49
	v_add_f32_e32 v50, v148, v50
	v_add_f32_e32 v51, v149, v51
	v_exp_f32_e32 v175, v93
	v_exp_f32_e32 v77, v77
	v_exp_f32_e32 v76, v109
	v_exp_f32_e32 v174, v61
	v_add_f32_e32 v48, v72, v48
	v_add_f32_e32 v49, v73, v49
	v_add_f32_e32 v50, v150, v50
	v_add_f32_e32 v51, v151, v51
	v_exp_f32_e32 v177, v94
	v_exp_f32_e32 v93, v78
	v_exp_f32_e32 v92, v110
	v_exp_f32_e32 v176, v62
	v_add_f32_e32 v48, v88, v48
	v_add_f32_e32 v49, v89, v49
	v_add_f32_e32 v50, v168, v50
	v_add_f32_e32 v51, v169, v51
	v_exp_f32_e32 v179, v95
	v_exp_f32_e32 v79, v79
	v_exp_f32_e32 v78, v111
	v_exp_f32_e32 v178, v63
	v_add_f32_e32 v48, v74, v48
	v_add_f32_e32 v49, v75, v49
	v_add_f32_e32 v50, v170, v50
	v_add_f32_e32 v51, v171, v51
	v_add_f32_e32 v48, v90, v48
	v_add_f32_e32 v49, v91, v49
	v_add_f32_e32 v50, v172, v50
	v_add_f32_e32 v51, v173, v51
	v_add_f32_e32 v48, v76, v48
	v_add_f32_e32 v49, v77, v49
	v_add_f32_e32 v50, v174, v50
	v_add_f32_e32 v51, v175, v51
	v_add_f32_e32 v48, v92, v48
	v_add_f32_e32 v49, v93, v49
	v_add_f32_e32 v50, v176, v50
	v_add_f32_e32 v51, v177, v51
	v_add_f32_e32 v48, v78, v48
	v_add_f32_e32 v49, v79, v49
	v_add_f32_e32 v50, v178, v50
	v_add_f32_e32 v51, v179, v51
	v_cvt_pk_bf16_f32 v57, v143, v67
	v_add_f32_e32 v48, v50, v48
	v_add_f32_e32 v49, v51, v49
	v_cvt_pk_bf16_f32 v67, v146, v70
	v_cvt_pk_bf16_f32 v70, v90, v76
	v_add3_u32 v76, s74, v162, v163
	v_add_f32_e32 v48, v48, v49
	v_cvt_pk_bf16_f32 v56, v141, v65
	v_cvt_pk_bf16_f32 v65, v142, v66
	v_cvt_pk_bf16_f32 v66, v144, v68
	v_cvt_pk_bf16_f32 v68, v102, v72
	v_cvt_pk_bf16_f32 v72, v138, v80
	v_add3_u32 v138, v76, v165, v157
	v_add_f32_e32 v161, v161, v48
	v_cvt_pk_bf16_f32 v48, v139, v81
	v_cvt_pk_bf16_f32 v49, v97, v83
	v_cvt_pk_bf16_f32 v50, v99, v85
	v_cvt_pk_bf16_f32 v51, v101, v87
	v_cvt_pk_bf16_f32 v58, v145, v69
	v_cvt_pk_bf16_f32 v59, v147, v71
	v_cvt_pk_bf16_f32 v60, v103, v73
	v_cvt_pk_bf16_f32 v61, v89, v75
	v_cvt_pk_bf16_f32 v62, v91, v77
	v_cvt_pk_bf16_f32 v63, v93, v79
	v_cvt_pk_bf16_f32 v69, v88, v74
	v_cvt_pk_bf16_f32 v71, v92, v78
	v_cvt_pk_bf16_f32 v73, v96, v82
	v_cvt_pk_bf16_f32 v74, v98, v84
	v_cvt_pk_bf16_f32 v75, v100, v86
	s_waitcnt vmcnt(0)
; #define LAS __attribute__((address_space(3)))
; __device__ __forceinline__ s16x4 vtr(const LAS unsigned char* p) { return __builtin_bit_cast(s16x4, __builtin_amdgcn_ds_read_tr16_b64_v4i16((LAS v4i16_t*)p)); }
; __device__ __forceinline__ void softmax_pv2(f32x16& a0, f32x16& a1, f32x16& b0, f32x16& b1, f32x16 (&o)[2], float& mref, float& l, f32x16& cn, bool first, LAS float* wsf, ...
;     ...
;     const int voff = (4 * hi + ((lane & 15) >> 2)) * 64 + ((lane >> 4) & 1) * 32 + (lane & 3) * 8;
; #pragma unroll
;     for (int t = 0; t < 2; ++t) { const LAS unsigned char* vb = (t == 0 ? VsA : VsB) + voff;
;         s16x4 lo[8], hh[8];
; #pragma unroll
;         for (int db = 0; db < 2; ++db)
; #pragma unroll
;             for (int ks = 0; ks < 4; ++ks) { lo[db * 4 + ks] = vtr(vb + db * 4096 + ks * 1024); hh[db * 4 + ks] = vtr(vb + db * 4096 + ks * 1024 + 512); }
;         __builtin_amdgcn_sched_barrier(0);
;     #pragma unroll
;         for (int ks = 0; ks < 4; ++ks)
; #pragma unroll
;             for (int db = 0; db < 2; ++db) { const int i = db * 4 + ks;
;                 const bf16x8 vf = (bf16x8){lo[i][0], lo[i][1], lo[i][2], lo[i][3], hh[i][0], hh[i][1], hh[i][2], hh[i][3]};
;                 o[db] = __builtin_amdgcn_mfma_f32_32x32x16_bf16(pa[4 * t + ks], vf, o[db], 0, 0, 0); }
;         }
	ds_read_b64_tr_b16 v[76:77], v138 offset:8192
	ds_read_b64_tr_b16 v[78:79], v138 offset:8704
	ds_read_b64_tr_b16 v[80:81], v138 offset:9216
	ds_read_b64_tr_b16 v[82:83], v138 offset:9728
	ds_read_b64_tr_b16 v[84:85], v138 offset:10240
	ds_read_b64_tr_b16 v[86:87], v138 offset:10752
	ds_read_b64_tr_b16 v[88:89], v138 offset:11264
	ds_read_b64_tr_b16 v[90:91], v138 offset:11776
	ds_read_b64_tr_b16 v[92:93], v138 offset:12288
	ds_read_b64_tr_b16 v[94:95], v138 offset:12800
	ds_read_b64_tr_b16 v[96:97], v138 offset:13312
	ds_read_b64_tr_b16 v[98:99], v138 offset:13824
	ds_read_b64_tr_b16 v[100:101], v138 offset:14336
	ds_read_b64_tr_b16 v[102:103], v138 offset:14848
	ds_read_b64_tr_b16 v[104:105], v138 offset:15360
	ds_read_b64_tr_b16 v[106:107], v138 offset:15872
	v_cvt_pk_bf16_f32 v52, v149, v151
	v_cvt_pk_bf16_f32 v53, v169, v171
	v_cvt_pk_bf16_f32 v54, v173, v175
	v_cvt_pk_bf16_f32 v55, v177, v179
	v_cvt_pk_bf16_f32 v64, v140, v64
	v_cvt_pk_bf16_f32 v108, v148, v150
	v_cvt_pk_bf16_f32 v109, v168, v170
	v_cvt_pk_bf16_f32 v110, v172, v174
	v_cvt_pk_bf16_f32 v111, v176, v178
	s_waitcnt lgkmcnt(14)
	v_mfma_f32_32x32x16_bf16 v[16:31], v[48:51], v[76:79], v[16:31]
	s_waitcnt lgkmcnt(6)
	v_mfma_f32_32x32x16_bf16 v[0:15], v[48:51], v[92:95], v[0:15]
	v_mfma_f32_32x32x16_bf16 v[16:31], v[52:55], v[80:83], v[16:31]
	s_waitcnt lgkmcnt(4)
	v_mfma_f32_32x32x16_bf16 v[0:15], v[52:55], v[96:99], v[0:15]
	v_mfma_f32_32x32x16_bf16 v[16:31], v[56:59], v[84:87], v[16:31]
	s_waitcnt lgkmcnt(2)
	v_mfma_f32_32x32x16_bf16 v[0:15], v[56:59], v[100:103], v[0:15]
	ds_read_b64_tr_b16 v[48:49], v138 offset:24576
	ds_read_b64_tr_b16 v[50:51], v138 offset:25088
	ds_read_b64_tr_b16 v[52:53], v138 offset:25600
	ds_read_b64_tr_b16 v[54:55], v138 offset:26112
	ds_read_b64_tr_b16 v[56:57], v138 offset:26624
	ds_read_b64_tr_b16 v[58:59], v138 offset:27136
	ds_read_b64_tr_b16 v[76:77], v138 offset:27648
	ds_read_b64_tr_b16 v[78:79], v138 offset:28160
	v_mfma_f32_32x32x16_bf16 v[16:31], v[60:63], v[88:91], v[16:31]
	ds_read_b64_tr_b16 v[80:81], v138 offset:28672
	ds_read_b64_tr_b16 v[82:83], v138 offset:29184
	ds_read_b64_tr_b16 v[84:85], v138 offset:29696
	ds_read_b64_tr_b16 v[86:87], v138 offset:30208
	ds_read_b64_tr_b16 v[88:89], v138 offset:30720
	ds_read_b64_tr_b16 v[90:91], v138 offset:31232
	ds_read_b64_tr_b16 v[92:93], v138 offset:31744
	ds_read_b64_tr_b16 v[94:95], v138 offset:32256
	s_waitcnt lgkmcnt(14)
	v_mfma_f32_32x32x16_bf16 v[0:15], v[60:63], v[104:107], v[0:15]
	v_mfma_f32_32x32x16_bf16 v[16:31], v[64:67], v[48:51], v[16:31]
	s_waitcnt lgkmcnt(6)
	v_mfma_f32_32x32x16_bf16 v[0:15], v[64:67], v[80:83], v[0:15]
	v_mfma_f32_32x32x16_bf16 v[16:31], v[68:71], v[52:55], v[16:31]
	s_waitcnt lgkmcnt(4)
	v_mfma_f32_32x32x16_bf16 v[0:15], v[68:71], v[84:87], v[0:15]
	v_mfma_f32_32x32x16_bf16 v[16:31], v[72:75], v[56:59], v[16:31]
	s_waitcnt lgkmcnt(2)
	v_mfma_f32_32x32x16_bf16 v[0:15], v[72:75], v[88:91], v[0:15]
	v_mfma_f32_32x32x16_bf16 v[16:31], v[108:111], v[76:79], v[16:31]
	s_waitcnt lgkmcnt(0)
	v_mfma_f32_32x32x16_bf16 v[0:15], v[108:111], v[92:95], v[0:15]

; #define LAS __attribute__((address_space(3)))
; __device__ __forceinline__ void moba_unit(const MobaArgs& A, int b, int h, int qb, LAS unsigned char* lds, int wave, bool tables) {
;     ...
;             if (near) {
;                 const LAS float* lp = lut + (LUTA_TOP - qpos + kt0 + 4 * hi);
; #pragma unroll
;                 for (int r = 0; r < 16; ++r) { const int c = (r & 3) + 8 * (r >> 2); a0[r] += lp[c]; a1[r] += lp[c + 32]; b0[r] += lp[c + 64]; b1[r] += lp[c + 96]; }
;                 if (own && kt0 + 127 > qmin) {
;                     const int lim = qpos - kt0 - 4 * hi;
; #pragma unroll
;                     for (int r = 0; r < 16; ++r) { const int c = (r & 3) + 8 * (r >> 2); if (c > lim) a0[r] = NEG; if (c + 32 > lim) a1[r] = NEG; if (c + 64 > lim) b0[r] = NEG; if (c + 96 > lim) b1[r] = NEG; }
.LBB0_745:
	s_andn2_b64 vcc, exec, s[10:11]
	s_cbranch_vccnz .LBB0_748
	v_sub_u32_e32 v138, s16, v132
	v_lshl_add_u32 v167, v138, 2, v166
	v_add_u32_e32 v167, 0x10fc, v167
	ds_read2_b32 v[168:169], v167 offset1:1
	ds_read2_b32 v[170:171], v167 offset0:32 offset1:33
	ds_read2_b32 v[172:173], v167 offset0:64 offset1:65
	ds_read2_b32 v[138:139], v167 offset0:96 offset1:97
	ds_read2_b32 v[174:175], v167 offset0:2 offset1:3
	ds_read2_b32 v[176:177], v167 offset0:34 offset1:35
	ds_read2_b32 v[178:179], v167 offset0:66 offset1:67
	ds_read2_b32 v[140:141], v167 offset0:98 offset1:99
	ds_read2_b32 v[180:181], v167 offset0:8 offset1:9
	ds_read2_b32 v[182:183], v167 offset0:40 offset1:41
	ds_read2_b32 v[184:185], v167 offset0:72 offset1:73
	ds_read2_b32 v[142:143], v167 offset0:104 offset1:105
	ds_read2_b32 v[186:187], v167 offset0:10 offset1:11
	ds_read2_b32 v[188:189], v167 offset0:42 offset1:43
	ds_read2_b32 v[190:191], v167 offset0:74 offset1:75
	ds_read2_b32 v[144:145], v167 offset0:106 offset1:107
	ds_read2_b32 v[192:193], v167 offset0:16 offset1:17
	ds_read2_b32 v[194:195], v167 offset0:48 offset1:49
	ds_read2_b32 v[196:197], v167 offset0:80 offset1:81
	ds_read2_b32 v[146:147], v167 offset0:112 offset1:113
	ds_read2_b32 v[198:199], v167 offset0:18 offset1:19
	ds_read2_b32 v[200:201], v167 offset0:50 offset1:51
	ds_read2_b32 v[202:203], v167 offset0:82 offset1:83
	ds_read2_b32 v[148:149], v167 offset0:114 offset1:115
	ds_read2_b32 v[204:205], v167 offset0:24 offset1:25
	ds_read2_b32 v[206:207], v167 offset0:56 offset1:57
	ds_read2_b32 v[208:209], v167 offset0:88 offset1:89
	ds_read2_b32 v[150:151], v167 offset0:120 offset1:121
	ds_read2_b32 v[210:211], v167 offset0:26 offset1:27
	s_waitcnt lgkmcnt(0)
	v_add_f32_e32 v80, v80, v168
	v_add_f32_e32 v81, v81, v169
	ds_read2_b32 v[168:169], v167 offset0:58 offset1:59
	s_cmp_ge_i32 s92, s17
	s_cselect_b64 s[6:7], -1, 0
	s_waitcnt lgkmcnt(0)
	v_add_f32_e32 v78, v78, v168
	v_add_f32_e32 v79, v79, v169
	ds_read2_b32 v[168:169], v167 offset0:90 offset1:91
	s_xor_b64 s[8:9], s[8:9], -1
	s_or_b64 s[6:7], s[8:9], s[6:7]
	v_add_f32_e32 v92, v92, v204
	v_add_f32_e32 v93, v93, v205
	v_add_f32_e32 v90, v90, v198
	v_add_f32_e32 v91, v91, v199
	s_waitcnt lgkmcnt(0)
	v_add_f32_e32 v110, v110, v168
	v_add_f32_e32 v111, v111, v169
	ds_read2_b32 v[168:169], v167 offset0:122 offset1:123
	v_add_f32_e32 v94, v94, v210
	v_add_f32_e32 v95, v95, v211
	v_add_f32_e32 v88, v88, v192
	v_add_f32_e32 v89, v89, v193
	v_add_f32_e32 v86, v86, v186
	v_add_f32_e32 v87, v87, v187
	v_add_f32_e32 v84, v84, v180
	v_add_f32_e32 v85, v85, v181
	v_add_f32_e32 v82, v82, v174
	v_add_f32_e32 v83, v83, v175
	v_add_f32_e32 v76, v76, v206
	v_add_f32_e32 v77, v77, v207
	v_add_f32_e32 v74, v74, v200
	v_add_f32_e32 v75, v75, v201
	v_add_f32_e32 v72, v72, v194
	v_add_f32_e32 v73, v73, v195
	v_add_f32_e32 v70, v70, v188
	v_add_f32_e32 v71, v71, v189
	v_add_f32_e32 v68, v68, v182
	v_add_f32_e32 v69, v69, v183
	v_add_f32_e32 v66, v66, v176
	v_add_f32_e32 v67, v67, v177
	v_add_f32_e32 v64, v64, v170
	v_add_f32_e32 v65, v65, v171
	v_add_f32_e32 v108, v108, v208
	v_add_f32_e32 v109, v109, v209
	v_add_f32_e32 v106, v106, v202
	v_add_f32_e32 v107, v107, v203
	v_add_f32_e32 v104, v104, v196
	v_add_f32_e32 v105, v105, v197
	v_add_f32_e32 v102, v102, v190
	v_add_f32_e32 v103, v103, v191
	v_add_f32_e32 v100, v100, v184
	v_add_f32_e32 v101, v101, v185
	v_add_f32_e32 v98, v98, v178
	v_add_f32_e32 v99, v99, v179
	v_add_f32_e32 v96, v96, v172
	v_add_f32_e32 v97, v97, v173
	s_waitcnt lgkmcnt(0)
	v_add_f32_e32 v62, v62, v168
	v_add_f32_e32 v63, v63, v169
	v_add_f32_e32 v60, v60, v150
	v_add_f32_e32 v61, v61, v151
	v_add_f32_e32 v58, v58, v148
	v_add_f32_e32 v59, v59, v149
	v_add_f32_e32 v56, v56, v146
	v_add_f32_e32 v57, v57, v147
	v_add_f32_e32 v54, v54, v144
	v_add_f32_e32 v55, v55, v145
	v_add_f32_e32 v52, v52, v142
	v_add_f32_e32 v53, v53, v143
	v_add_f32_e32 v50, v50, v140
	v_add_f32_e32 v51, v51, v141
	v_add_f32_e32 v48, v48, v138
	v_add_f32_e32 v49, v49, v139
	s_and_b64 vcc, exec, s[6:7]
	s_cbranch_vccnz .LBB0_748
	v_add_u32_e32 v138, s16, v160
	v_sub_u32_e32 v138, v132, v138
	v_cmp_gt_i32_e64 s[44:45], 26, v138
	v_cmp_gt_i32_e64 s[60:61], 27, v138
	s_and_b64 s[44:45], s[60:61], s[44:45]
	v_cndmask_b32_e64 v94, v94, v252, s[44:45]
	v_cndmask_b32_e64 v95, v95, v252, s[60:61]
	v_cmp_gt_i32_e64 s[60:61], 25, v138
	s_and_b64 s[44:45], s[44:45], s[60:61]
	v_cmp_gt_i32_e64 s[60:61], 24, v138
	v_cndmask_b32_e64 v93, v93, v252, s[44:45]
	s_and_b64 s[44:45], s[44:45], s[60:61]
	v_cmp_gt_i32_e64 s[60:61], 19, v138
	v_cndmask_b32_e64 v92, v92, v252, s[44:45]
	s_and_b64 s[44:45], s[44:45], s[60:61]
	v_cmp_gt_i32_e64 s[60:61], 18, v138
	v_cndmask_b32_e64 v91, v91, v252, s[44:45]
	s_and_b64 s[44:45], s[44:45], s[60:61]
	v_cmp_gt_i32_e64 s[60:61], 17, v138
	v_cndmask_b32_e64 v90, v90, v252, s[44:45]
	s_and_b64 s[44:45], s[44:45], s[60:61]
	v_cmp_gt_i32_e64 s[60:61], 16, v138
	v_cndmask_b32_e64 v89, v89, v252, s[44:45]
	s_and_b64 s[44:45], s[44:45], s[60:61]
	v_cmp_gt_i32_e64 s[60:61], 11, v138
	v_cmp_gt_i32_e64 s[28:29], 10, v138
	s_and_b64 s[60:61], s[44:45], s[60:61]
	v_cmp_gt_i32_e64 s[58:59], 9, v138
	v_cndmask_b32_e64 v87, v87, v252, s[60:61]
	s_and_b64 s[60:61], s[60:61], s[28:29]
	v_cmp_gt_i32_e64 s[50:51], 8, v138
	v_cndmask_b32_e64 v86, v86, v252, s[60:61]
	s_and_b64 s[60:61], s[60:61], s[58:59]
	v_cmp_gt_i32_e64 s[36:37], 3, v138
	v_cndmask_b32_e64 v85, v85, v252, s[60:61]
	s_and_b64 s[60:61], s[60:61], s[50:51]
	v_cmp_gt_i32_e64 s[56:57], 2, v138
	v_cndmask_b32_e64 v84, v84, v252, s[60:61]
	s_and_b64 s[60:61], s[60:61], s[36:37]
	v_cmp_gt_i32_e64 s[52:53], 1, v138
; __device__ __forceinline__ void moba_unit(const MobaArgs& A, int b, int h, int qb, LAS unsigned char* lds, int wave, bool tables) {
;     ...
;                 if (own && kt0 + 127 > qmin) {
;                     const int lim = qpos - kt0 - 4 * hi;
; #pragma unroll
;                     for (int r = 0; r < 16; ++r) { const int c = (r & 3) + 8 * (r >> 2); if (c > lim) a0[r] = NEG; if (c + 32 > lim) a1[r] = NEG; if (c + 64 > lim) b0[r] = NEG; if (c + 96 > lim) b1[r] = NEG; }
;                 }
	v_cndmask_b32_e64 v83, v83, v252, s[60:61]
	s_and_b64 s[60:61], s[60:61], s[56:57]
	v_cmp_gt_i32_e64 s[54:55], 0, v138
	v_cndmask_b32_e64 v82, v82, v252, s[60:61]
	s_and_b64 s[60:61], s[60:61], s[52:53]
	s_and_b64 s[54:55], s[60:61], s[54:55]
	v_cndmask_b32_e64 v81, v81, v252, s[60:61]
	v_cmp_gt_i32_e64 s[60:61], 58, v138
	v_cndmask_b32_e64 v80, v80, v252, s[54:55]
	v_cmp_gt_i32_e64 s[54:55], 59, v138
	v_cmp_gt_i32_e64 s[56:57], 48, v138
	v_cmp_gt_i32_e64 s[58:59], 43, v138
	v_cndmask_b32_e64 v79, v79, v252, s[54:55]
	s_and_b64 s[54:55], s[54:55], s[60:61]
	v_cmp_gt_i32_e64 s[60:61], 57, v138
	v_cndmask_b32_e64 v78, v78, v252, s[54:55]
	s_and_b64 s[54:55], s[54:55], s[60:61]
	v_cmp_gt_i32_e64 s[60:61], 56, v138
	v_cndmask_b32_e64 v77, v77, v252, s[54:55]
	s_and_b64 s[54:55], s[54:55], s[60:61]
	v_cmp_gt_i32_e64 s[60:61], 51, v138
	v_cndmask_b32_e64 v76, v76, v252, s[54:55]
	s_and_b64 s[54:55], s[54:55], s[60:61]
	v_cmp_gt_i32_e64 s[60:61], 50, v138
	v_cndmask_b32_e64 v75, v75, v252, s[54:55]
	s_and_b64 s[54:55], s[54:55], s[60:61]
	v_cmp_gt_i32_e64 s[60:61], 49, v138
	s_and_b64 s[60:61], s[54:55], s[60:61]
	s_and_b64 s[56:57], s[60:61], s[56:57]
	v_cmp_gt_i32_e64 s[48:49], 42, v138
	s_and_b64 s[58:59], s[56:57], s[58:59]
	v_cmp_gt_i32_e64 s[46:47], 41, v138
	v_cndmask_b32_e64 v71, v71, v252, s[58:59]
	s_and_b64 s[58:59], s[58:59], s[48:49]
	v_cmp_gt_i32_e64 s[42:43], 40, v138
	v_cndmask_b32_e64 v70, v70, v252, s[58:59]
	s_and_b64 s[58:59], s[58:59], s[46:47]
	v_cmp_gt_i32_e64 s[40:41], 35, v138
	v_cndmask_b32_e64 v69, v69, v252, s[58:59]
	s_and_b64 s[58:59], s[58:59], s[42:43]
	v_cmp_gt_i32_e64 s[38:39], 34, v138
	v_cndmask_b32_e64 v68, v68, v252, s[58:59]
	s_and_b64 s[58:59], s[58:59], s[40:41]
	v_cmp_gt_i32_e64 s[34:35], 33, v138
	s_and_b64 s[38:39], s[58:59], s[38:39]
	v_cmp_gt_i32_e64 s[30:31], 32, v138
	v_cndmask_b32_e64 v66, v66, v252, s[38:39]
	s_and_b64 s[38:39], s[38:39], s[34:35]
	s_and_b64 s[30:31], s[38:39], s[30:31]
	v_cndmask_b32_e64 v65, v65, v252, s[38:39]
	s_movk_i32 s38, 0x5a
	v_cndmask_b32_e64 v64, v64, v252, s[30:31]
	s_movk_i32 s30, 0x5b
	v_cmp_gt_i32_e64 s[38:39], s38, v138
	v_cmp_gt_i32_e64 s[30:31], s30, v138
	v_cndmask_b32_e64 v67, v67, v252, s[58:59]
	s_movk_i32 s58, 0x58
	v_cndmask_b32_e64 v111, v111, v252, s[30:31]
	s_and_b64 s[30:31], s[30:31], s[38:39]
	s_movk_i32 s38, 0x59
	v_cmp_gt_i32_e64 s[38:39], s38, v138
	s_movk_i32 s42, 0x53
	v_cmp_gt_i32_e64 s[58:59], s58, v138
	v_cndmask_b32_e64 v110, v110, v252, s[30:31]
	s_and_b64 s[30:31], s[30:31], s[38:39]
	s_movk_i32 s48, 0x52
	v_cmp_gt_i32_e64 s[42:43], s42, v138
	v_cndmask_b32_e64 v109, v109, v252, s[30:31]
	s_and_b64 s[30:31], s[30:31], s[58:59]
	v_cndmask_b32_e64 v73, v73, v252, s[60:61]
	s_movk_i32 s60, 0x51
	v_cmp_gt_i32_e64 s[48:49], s48, v138
	v_cndmask_b32_e64 v108, v108, v252, s[30:31]
	s_and_b64 s[30:31], s[30:31], s[42:43]
	s_movk_i32 s52, 0x50
	v_cmp_gt_i32_e64 s[60:61], s60, v138
	v_cndmask_b32_e64 v107, v107, v252, s[30:31]
	s_and_b64 s[30:31], s[30:31], s[48:49]
	s_movk_i32 s50, 0x4b
	v_cmp_gt_i32_e64 s[52:53], s52, v138
	v_cndmask_b32_e64 v106, v106, v252, s[30:31]
	s_and_b64 s[30:31], s[30:31], s[60:61]
	v_cndmask_b32_e64 v88, v88, v252, s[44:45]
	s_movk_i32 s44, 0x4a
	v_cmp_gt_i32_e64 s[50:51], s50, v138
	v_cndmask_b32_e64 v105, v105, v252, s[30:31]
	s_and_b64 s[30:31], s[30:31], s[52:53]
	s_movk_i32 s14, 0x49
	v_cmp_gt_i32_e64 s[44:45], s44, v138
	v_cndmask_b32_e64 v104, v104, v252, s[30:31]
	s_and_b64 s[30:31], s[30:31], s[50:51]
	s_movk_i32 s12, 0x48
	v_cmp_gt_i32_e64 s[26:27], s14, v138
	v_cndmask_b32_e64 v103, v103, v252, s[30:31]
	s_and_b64 s[30:31], s[30:31], s[44:45]
	s_movk_i32 s10, 0x43
	v_cmp_gt_i32_e64 s[24:25], s12, v138
	s_and_b64 s[26:27], s[30:31], s[26:27]
	s_movk_i32 s6, 0x60
	s_movk_i32 s8, 0x42
	v_cmp_gt_i32_e64 s[22:23], s10, v138
	s_and_b64 s[24:25], s[26:27], s[24:25]
	v_cmp_gt_i32_e32 vcc, s6, v138
	s_movk_i32 s6, 0x41
	v_cmp_gt_i32_e64 s[20:21], s8, v138
	s_and_b64 s[22:23], s[24:25], s[22:23]
	v_cmp_gt_i32_e64 s[18:19], s6, v138
	s_and_b64 s[20:21], s[22:23], s[20:21]
	v_cmp_gt_i32_e64 s[16:17], 64, v138
	s_and_b64 s[18:19], s[20:21], s[18:19]
	s_and_b64 s[16:17], s[18:19], s[16:17]
	s_movk_i32 s58, 0x7a
	v_cndmask_b32_e64 v96, v96, v252, s[16:17]
	s_movk_i32 s16, 0x7b
	s_movk_i32 s38, 0x79
	v_cmp_gt_i32_e64 s[58:59], s58, v138
	v_cmp_gt_i32_e64 s[16:17], s16, v138
	s_movk_i32 s34, 0x78
	v_cmp_gt_i32_e64 s[38:39], s38, v138
	v_cndmask_b32_e64 v63, v63, v252, s[16:17]
	s_and_b64 s[16:17], s[16:17], s[58:59]
	s_movk_i32 s40, 0x73
	v_cmp_gt_i32_e64 s[34:35], s34, v138
	v_cndmask_b32_e64 v62, v62, v252, s[16:17]
	s_and_b64 s[16:17], s[16:17], s[38:39]
	s_movk_i32 s46, 0x72
	v_cmp_gt_i32_e64 s[40:41], s40, v138
	v_cndmask_b32_e64 v61, v61, v252, s[16:17]
	s_and_b64 s[16:17], s[16:17], s[34:35]
	v_cndmask_b32_e64 v72, v72, v252, s[56:57]
	s_movk_i32 s56, 0x71
	v_cmp_gt_i32_e64 s[46:47], s46, v138
	v_cndmask_b32_e64 v60, v60, v252, s[16:17]
	s_and_b64 s[16:17], s[16:17], s[40:41]
	v_cndmask_b32_e64 v74, v74, v252, s[54:55]
	s_movk_i32 s54, 0x70
	v_cmp_gt_i32_e64 s[56:57], s56, v138
	v_cndmask_b32_e64 v59, v59, v252, s[16:17]
	s_and_b64 s[16:17], s[16:17], s[46:47]
	s_movk_i32 s36, 0x6b
	v_cmp_gt_i32_e64 s[54:55], s54, v138
	v_cndmask_b32_e64 v58, v58, v252, s[16:17]
	s_and_b64 s[16:17], s[16:17], s[56:57]
	s_movk_i32 s28, 0x6a
	v_cmp_gt_i32_e64 s[36:37], s36, v138
	v_cndmask_b32_e64 v57, v57, v252, s[16:17]
	s_and_b64 s[16:17], s[16:17], s[54:55]
	s_movk_i32 s14, 0x69
	v_cmp_gt_i32_e64 s[28:29], s28, v138
	v_cndmask_b32_e64 v56, v56, v252, s[16:17]
	s_and_b64 s[16:17], s[16:17], s[36:37]
	s_movk_i32 s12, 0x68
	v_cmp_gt_i32_e64 s[14:15], s14, v138
	v_cndmask_b32_e64 v55, v55, v252, s[16:17]
	s_and_b64 s[16:17], s[16:17], s[28:29]
	s_movk_i32 s10, 0x63
	v_cmp_gt_i32_e64 s[12:13], s12, v138
	s_and_b64 s[14:15], s[16:17], s[14:15]
	s_movk_i32 s8, 0x62
	v_cmp_gt_i32_e64 s[10:11], s10, v138
	s_and_b64 s[12:13], s[14:15], s[12:13]
	s_movk_i32 s6, 0x61
	v_cmp_gt_i32_e64 s[8:9], s8, v138
	s_and_b64 s[10:11], s[12:13], s[10:11]
	v_cmp_gt_i32_e64 s[6:7], s6, v138
	s_and_b64 s[8:9], s[10:11], s[8:9]
	s_and_b64 s[6:7], s[8:9], s[6:7]
	s_and_b64 vcc, s[6:7], vcc
	s_mov_b32 s61, 0xe000
	s_mov_b32 s60, 0xc000
	v_cndmask_b32_e64 v102, v102, v252, s[30:31]
	v_cndmask_b32_e64 v101, v101, v252, s[26:27]
	v_cndmask_b32_e64 v100, v100, v252, s[24:25]
	v_cndmask_b32_e64 v99, v99, v252, s[22:23]
	v_cndmask_b32_e64 v98, v98, v252, s[20:21]
	v_cndmask_b32_e64 v97, v97, v252, s[18:19]
	v_cndmask_b32_e64 v54, v54, v252, s[16:17]
	v_cndmask_b32_e64 v53, v53, v252, s[14:15]
	v_cndmask_b32_e64 v52, v52, v252, s[12:13]
	v_cndmask_b32_e64 v51, v51, v252, s[10:11]
	v_cndmask_b32_e64 v50, v50, v252, s[8:9]
	v_cndmask_b32_e64 v49, v49, v252, s[6:7]
	v_cndmask_b32_e32 v48, v48, v252, vcc
